# GQA: key tiles that lie wholly inside the +-128 band skip the band-mask arithmetic (wave-uniform test, unmasked path)
# baseline (speedup 1.0000x reference)
.LBB0_618:
	s_add_i32 s70, s63, s67
	s_add_i32 s2, s70, 63
	s_add_i32 s71, s65, 0x100
	s_cmp_gt_i32 s2, s71
	s_cbranch_scc1 .Lgq_nf0
	s_add_i32 s71, s66, 0xffffff00
	s_cmp_lt_i32 s70, s71
	s_cbranch_scc1 .Lgq_nf0
	s_mov_b64 s[22:23], -1
.Lgq_nf0:
	s_cmp_ge_i32 s2, s65
	s_cselect_b64 s[2:3], -1, 0
	s_cmp_le_u32 s70, s66
	s_cselect_b64 s[70:71], -1, 0
	s_and_b64 s[2:3], s[2:3], s[70:71]
	s_andn2_b64 vcc, exec, s[2:3]
	s_and_b32 s69, s69, 1
	s_cbranch_vccnz .LBB0_614

.LBB0_1914:
	s_add_i32 s68, s64, s63
	s_add_i32 s18, s68, 63
	s_add_i32 s69, s61, 0x100
	s_cmp_gt_i32 s18, s69
	s_cbranch_scc1 .Lgq_nf1
	s_add_i32 s69, s62, 0xffffff00
	s_cmp_lt_i32 s68, s69
	s_cbranch_scc1 .Lgq_nf1
	s_mov_b64 s[16:17], 0
.Lgq_nf1:
	s_cmp_ge_i32 s18, s61
	s_cselect_b64 s[18:19], -1, 0
	s_cmp_le_u32 s68, s62
	s_cselect_b64 s[68:69], -1, 0
	s_and_b64 s[18:19], s[18:19], s[68:69]
	s_andn2_b64 vcc, exec, s[18:19]
	s_and_b32 s67, s67, 1
	s_cbranch_vccnz .LBB0_1910
